# agg tail: LayerNorm parameter loads issued at the top of the tail (overlap the division / conversions / reductions); header no longer waits for the self row
# baseline (speedup 1.0000x reference)
_Z7agg_ln1PKDF16_S0_S0_PKiS2_S2_PKfS4_S4_PDF16_S4_S4_S5_S5_:
	s_cmpk_gt_u32 s2, 0xff
	s_mov_b64 s[4:5], -1
	s_cbranch_scc0 .LBB1_28
	v_lshl_or_b32 v1, s2, 8, v0
	v_add_u32_e32 v1, 0xffff0000, v1
	s_mov_b32 s3, 0x9c400
	v_cmp_gt_u32_e32 vcc, s3, v1
	s_and_saveexec_b64 s[18:19], vcc
	s_cbranch_execz .LBB1_27
	s_load_dwordx2 s[4:5], s[0:1], 0x20
	s_load_dwordx2 s[6:7], s[0:1], 0x18
	s_load_dwordx2 s[32:33], s[0:1], 0x8
	v_lshrrev_b32_e32 v1, 6, v1
	v_lshlrev_b32_e32 v2, 4, v1
	v_and_b32_e32 v24, 63, v0
	v_lshlrev_b32_e32 v8, 3, v24
	v_lshlrev_b32_e32 v21, 10, v1
	v_lshl_add_u32 v21, v24, 4, v21
	s_waitcnt lgkmcnt(0)
	global_load_dwordx4 v[28:31], v2, s[6:7]
	global_load_dwordx4 v[2:5], v2, s[4:5]
	global_load_dwordx4 v[60:63], v21, s[32:33] nt
	s_waitcnt vmcnt(1)
	v_add_u32_e32 v26, v3, v2
	v_add_u32_e32 v3, v26, v4
	v_add_u32_e32 v25, v3, v5
	v_cmp_gt_i32_e32 vcc, 1, v25
	s_and_saveexec_b64 s[4:5], vcc
	s_xor_b64 s[4:5], exec, s[4:5]
	v_mov_b32_e32 v9, 0
	s_or_saveexec_b64 s[22:23], s[4:5]
	s_load_dwordx2 s[20:21], s[0:1], 0x48
	v_mov_b32_e32 v11, 0
	v_mov_b64_e32 v[18:19], 0
	v_mov_b32_e32 v10, v11
	v_mov_b32_e32 v13, v11
	v_mov_b32_e32 v12, v11
	v_mov_b32_e32 v15, v11
	v_mov_b32_e32 v14, v11
	v_mov_b32_e32 v17, v11
	v_mov_b32_e32 v16, v11
	s_xor_b64 exec, exec, s[22:23]
	s_cbranch_execz .LBB1_26
	s_load_dwordx2 s[24:25], s[0:1], 0x28
	s_load_dwordx2 s[26:27], s[0:1], 0x0
	v_readfirstlane_b32 s2, v25
	v_readfirstlane_b32 s4, v2
	v_readfirstlane_b32 s5, v26
	v_readfirstlane_b32 s6, v3
	v_readfirstlane_b32 s8, v28
	v_readfirstlane_b32 s9, v29
	v_readfirstlane_b32 s10, v30
	v_readfirstlane_b32 s11, v31
	v_lshrrev_b32_e32 v20, 3, v24
	v_lshlrev_b32_e32 v20, 2, v20
	v_mov_b32_e32 v9, 0
	v_mov_b32_e32 v10, 0
	v_mov_b32_e32 v11, 0
	v_mov_b32_e32 v12, 0
	v_mov_b32_e32 v13, 0
	v_mov_b32_e32 v14, 0
	v_mov_b32_e32 v15, 0
	v_mov_b32_e32 v16, 0
	v_mov_b32_e32 v17, 0
	s_sub_u32 s9, s9, s4
	s_sub_u32 s10, s10, s5
	s_sub_u32 s11, s11, s6
	s_mov_b64 s[12:13], 0
	s_mov_b32 s3, 0
	s_sub_u32 s7, s2, 1
	s_waitcnt lgkmcnt(0)

.LBB1_26:
	s_or_b64 exec, exec, s[22:23]
	s_load_dwordx2 s[8:9], s[0:1], 0x40
	s_load_dwordx2 s[10:11], s[0:1], 0x8
	s_load_dwordx4 s[4:7], s[0:1], 0x30
	v_lshlrev_b64 v[44:45], 2, v[8:9]
	v_lshlrev_b32_e32 v42, 10, v1
	v_mov_b32_e32 v43, 0
	s_waitcnt lgkmcnt(0)
	v_lshl_add_u64 v[22:23], s[6:7], 0, v[44:45]
	v_lshl_add_u64 v[44:45], s[8:9], 0, v[44:45]
	global_load_dwordx4 v[18:21], v[22:23], off
	global_load_dwordx4 v[34:37], v[22:23], off offset:16
	global_load_dwordx4 v[38:41], v[44:45], off offset:16
	v_max_i32_e32 v25, 1, v25
	v_cvt_f32_u32_e32 v25, v25
	v_div_scale_f32 v46, s[4:5], v25, v25, 1.0
	v_rcp_f32_e32 v52, v46
	v_div_scale_f32 v42, vcc, 1.0, v25, 1.0
	v_fma_f32 v53, -v46, v52, 1.0
	v_fmac_f32_e32 v52, v53, v52
	v_mul_f32_e32 v53, v42, v52
	v_fma_f32 v55, -v46, v53, v42
	v_fmac_f32_e32 v53, v55, v52
	v_fma_f32 v42, -v46, v53, v42
	v_div_fmas_f32 v42, v42, v52, v53
	v_div_fixup_f32 v42, v42, v25, 1.0
	s_waitcnt vmcnt(3)
	v_cvt_f32_f16_e32 v54, v60
	v_cvt_f32_f16_sdwa v55, v60 dst_sel:DWORD dst_unused:UNUSED_PAD src0_sel:WORD_1
	v_cvt_f32_f16_e32 v56, v61
	v_cvt_f32_f16_sdwa v57, v61 dst_sel:DWORD dst_unused:UNUSED_PAD src0_sel:WORD_1
	v_cvt_f32_f16_e32 v58, v62
	v_cvt_f32_f16_sdwa v59, v62 dst_sel:DWORD dst_unused:UNUSED_PAD src0_sel:WORD_1
	v_cvt_f32_f16_e32 v60, v63
	v_cvt_f32_f16_sdwa v61, v63 dst_sel:DWORD dst_unused:UNUSED_PAD src0_sel:WORD_1
	v_pk_fma_f32 v[22:23], v[16:17], v[42:43], v[54:55] op_sel_hi:[1,0,1]
	v_pk_fma_f32 v[54:55], v[14:15], v[42:43], v[56:57] op_sel_hi:[1,0,1]
	global_load_dwordx4 v[14:17], v[44:45], off
	v_mov_b32_e32 v44, v54
	v_mov_b32_e32 v45, v55
	v_pk_fma_f32 v[12:13], v[12:13], v[42:43], v[58:59] op_sel_hi:[1,0,1]
	v_mov_b32_e32 v25, 0x3b000000
	v_add_f32_e32 v6, 0, v22
	v_add_f32_e32 v6, v6, v23
	v_add_f32_e32 v6, v6, v44
	v_add_f32_e32 v6, v6, v45
	v_mov_b32_e32 v2, v12
	v_mov_b32_e32 v3, v13
	s_nop 0
	v_add_f32_e32 v6, v6, v2
	v_add_f32_e32 v12, v6, v3
	v_pk_fma_f32 v[6:7], v[10:11], v[42:43], v[60:61] op_sel_hi:[1,0,1]
	v_mov_b32_e32 v4, v6
	v_mov_b32_e32 v5, v7
	v_mov_b32_e32 v7, v43
	v_add_f32_e32 v6, v12, v4
	v_add_f32_e32 v6, v6, v5
	s_nop 1
	v_add_f32_dpp v6, v6, v6 quad_perm:[1,0,3,2] row_mask:0xf bank_mask:0xf bound_ctrl:1
	s_nop 1
	v_add_f32_dpp v6, v6, v6 quad_perm:[2,3,0,1] row_mask:0xf bank_mask:0xf bound_ctrl:1
	s_nop 1
	v_add_f32_dpp v6, v6, v6 row_half_mirror row_mask:0xf bank_mask:0xf bound_ctrl:1
	s_nop 1
	v_add_f32_dpp v6, v6, v6 row_mirror row_mask:0xf bank_mask:0xf bound_ctrl:1
	s_nop 1
	v_mov_b32_dpp v7, v6 row_bcast:15 row_mask:0xa bank_mask:0xf
	v_add_f32_e32 v6, v6, v7
	v_mov_b32_e32 v7, v43
	s_nop 1
	v_mov_b32_dpp v7, v6 row_bcast:31 row_mask:0xc bank_mask:0xf
	v_add_f32_e32 v6, v6, v7
	s_nop 0
	v_readlane_b32 s3, v6, 63
	s_nop 1
	v_mul_f32_e32 v6, s3, v25
	v_pk_add_f32 v[8:9], v[22:23], v[6:7] op_sel_hi:[1,0] neg_lo:[0,1] neg_hi:[0,1]
	v_pk_add_f32 v[12:13], v[44:45], v[6:7] op_sel_hi:[1,0] neg_lo:[0,1] neg_hi:[0,1]
	v_pk_mul_f32 v[10:11], v[8:9], v[8:9]
	v_pk_mul_f32 v[22:23], v[12:13], v[12:13]
	v_add_f32_e32 v10, v10, v11
	v_pk_add_f32 v[2:3], v[2:3], v[6:7] op_sel_hi:[1,0] neg_lo:[0,1] neg_hi:[0,1]
	v_add_f32_e32 v10, v10, v22
	v_pk_mul_f32 v[26:27], v[2:3], v[2:3]
	v_add_f32_e32 v10, v10, v23
	v_pk_add_f32 v[4:5], v[4:5], v[6:7] op_sel_hi:[1,0] neg_lo:[0,1] neg_hi:[0,1]
	v_add_f32_e32 v10, v10, v26
	v_pk_mul_f32 v[6:7], v[4:5], v[4:5]
	v_add_f32_e32 v10, v10, v27
	v_add_f32_e32 v6, v10, v6
	v_add_f32_e32 v6, v6, v7
	v_mov_b32_e32 v7, v43
	s_nop 0
	v_add_f32_dpp v6, v6, v6 quad_perm:[1,0,3,2] row_mask:0xf bank_mask:0xf bound_ctrl:1
	s_nop 1
	v_add_f32_dpp v6, v6, v6 quad_perm:[2,3,0,1] row_mask:0xf bank_mask:0xf bound_ctrl:1
	s_nop 1
	v_add_f32_dpp v6, v6, v6 row_half_mirror row_mask:0xf bank_mask:0xf bound_ctrl:1
	s_nop 1
	v_add_f32_dpp v6, v6, v6 row_mirror row_mask:0xf bank_mask:0xf bound_ctrl:1
	s_nop 1
	v_mov_b32_dpp v7, v6 row_bcast:15 row_mask:0xa bank_mask:0xf
	v_add_f32_e32 v6, v6, v7
	s_nop 1
	v_mov_b32_dpp v43, v6 row_bcast:31 row_mask:0xc bank_mask:0xf
	v_add_f32_e32 v6, v6, v43
	s_nop 0
	v_readlane_b32 s3, v6, 63
	v_mov_b32_e32 v6, 0x3727c5ac
	s_nop 0
	v_fmac_f32_e32 v6, s3, v25
	s_mov_b32 s3, 0x800000
	v_mul_f32_e32 v7, 0x4b800000, v6
	v_cmp_gt_f32_e32 vcc, s3, v6
	s_movk_i32 s3, 0x2800
	s_nop 0
	v_cndmask_b32_e32 v6, v6, v7, vcc
	v_rsq_f32_e32 v6, v6
	v_lshrrev_b32_e32 v7, 3, v24
	v_mad_u32_u24 v1, v7, s3, v1
	v_mul_f32_e32 v7, 0x45800000, v6
	v_cndmask_b32_e32 v6, v6, v7, vcc
	v_pk_mul_f32 v[2:3], v[2:3], v[6:7] op_sel_hi:[1,0]
	v_pk_mul_f32 v[10:11], v[12:13], v[6:7] op_sel_hi:[1,0]
	s_waitcnt vmcnt(0)
	v_pk_fma_f32 v[12:13], v[34:35], v[2:3], v[38:39]
	v_pk_mul_f32 v[2:3], v[4:5], v[6:7] op_sel_hi:[1,0]
	v_pk_mul_f32 v[8:9], v[8:9], v[6:7] op_sel_hi:[1,0]
	v_pk_fma_f32 v[6:7], v[36:37], v[2:3], v[40:41]
	v_pk_fma_f32 v[8:9], v[18:19], v[8:9], v[14:15]
	v_cvt_pk_f16_f32 v5, v6, v7
	v_lshlrev_b32_e32 v6, 4, v0
	v_pk_fma_f32 v[10:11], v[20:21], v[10:11], v[16:17]
	v_and_b32_e32 v6, 0x70, v6
	v_cvt_pk_f16_f32 v2, v8, v9
	v_cvt_pk_f16_f32 v3, v10, v11
	v_cvt_pk_f16_f32 v4, v12, v13
	v_lshl_or_b32 v1, v1, 7, v6
	global_store_dwordx4 v1, v[2:5], s[20:21]
